# accumulator clearing between GEMM units via zero-operand MFMAs (4 v_mov + 10 MFMA) instead of 128 v_mov
# speedup vs baseline: 1.0074x; 1.0023x over previous
; #define LAS __attribute__((address_space(3)))
; template <class Epi, class Sched, bool ALIGN_EPI, bool FP8 = false>
; DI void gemm_phase(LAS unsigned char* lds, const Gemm g, const Sched& S, const Epi& E) {
;     ...
;     const int wid = __builtin_amdgcn_readfirstlane(tid >> 6), lane = tid & 63, wr = wid >> 2, wc = wid & 3, fr = lane & 15, fq = lane >> 4;
;     const int K = g.K; int nt = K / BK;
;     unsigned voffA[2], voffB[2];
; #pragma unroll
;     for (int i = 0; i < 2; ++i) { int R, C; stage_rc(tid * 16 + i * 8192, R, C); const int Rb = Epi::PERM ? ((R & ~31) + perm32(R & 31)) : R;
;         voffA[i] = (unsigned)(R * g.lda + C) * 2u; voffB[i] = (unsigned)(Rb * g.ldb + C) * 2u; }
;     const size_t kstep = (size_t)(BK * 2);
;     const size_t hstepA = (size_t)HALF * g.lda * 2, hstepB = (size_t)HALF * g.ldb * 2;
;     const unsigned ldsw = (unsigned)wid * 1024u;
;     const unsigned ldsbase = (unsigned)__builtin_amdgcn_readfirstlane((int)(unsigned)(size_t)lds) + ldsw;
;     const int aoff = lds_byte(wr * 64 + fr, fq * 8), boff = lds_byte(wc * 32 + fr, fq * 8);
;     const int aoff8a = lds_byte(wr * 64 + fr, fq * 16), boff8a = lds_byte(wc * 32 + fr, fq * 16);
;     const LAS unsigned char* a8base = lds + aoff8a; const LAS unsigned char* b8base = lds + 4 * HTB + boff8a;
;     if constexpr (FP8) { asm volatile("" : "+v"(a8base)); asm volatile("" : "+v"(b8base)); }
;     static_assert(lds_byte(9, 24) == lds_byte(9, 16) + 16 && lds_byte(3, 56) == lds_byte(3, 48) + 16, "fp8 fragment pieces are adjacent");
;     ...
;     Unit cur, nxt; int ui = 0;
;     if (!S.next(0, cur)) return;
;     if constexpr (sched_vark<Sched>::value) nt = S.nt(cur);
;     f32x4 acc[2][2][4][2];
; #pragma unroll
;     for (int a = 0; a < 2; ++a)
; #pragma unroll
;         for (int b = 0; b < 2; ++b)
; #pragma unroll
;             for (int m = 0; m < 4; ++m)
; #pragma unroll
;                 for (int n = 0; n < 2; ++n) acc[a][b][m][n] = (f32x4){0.f, 0.f, 0.f, 0.f};
;     bf16x8 At[4][2], B0[2][2], B1[2][2]; v8i At8[4], B08[2], B18[2];
;     const char* cA = (const char*)g.A + S.a_off(cur); const char* cB = (const char*)g.Bt + S.b_off(cur);
;     PG8_STAGE(PG8_SB(0, 0), cB, voffB); PG8_STAGE(PG8_SB(0, 1), cB + hstepB, voffB); PG8_STAGE(PG8_SA(0, 0), cA, voffA); PG8_STAGE(PG8_SA(0, 1), cA + hstepA, voffA);
;     if (wr == 1) PG8_BAR;
;     PG8_WAIT_V(2); PG8_BAR;
.LBB0_226:
	s_and_b64 s[4:5], s[4:5], exec
	s_cselect_b32 s20, 32, 16
	s_and_b64 s[4:5], s[6:7], exec
	s_cselect_b32 s81, s20, 4
	s_add_u32 s74, s12, 0x18b00000
	s_addc_u32 s75, s13, 0
	v_bfe_u32 v2, v0, 4, 2
	s_add_u32 s79, s12, 0x1ab00000
	v_and_b32_e32 v1, 15, v0
	v_lshlrev_b32_e32 v130, 4, v2
	v_lshlrev_b32_e32 v0, 2, v0
	s_addc_u32 s80, s13, 0
	s_and_b32 s6, s8, 3
	v_lshl_or_b32 v156, s9, 6, v1
	s_lshl_b32 s4, s9, 13
	v_lshl_or_b32 v1, v1, 6, v130
	v_and_b32_e32 v0, 32, v0
	v_bitop3_b32 v4, v1, s4, v0 bitop3:0xde
	s_lshl_b32 s82, s6, 5
	s_lshl_b32 s4, s6, 12
	v_bitop3_b32 v1, v1, s4, v0 bitop3:0xde
	s_add_u32 s4, s22, 0x80
	s_waitcnt vmcnt(2)
	s_barrier
	s_addc_u32 s5, s23, 0
	s_add_i32 s83, s15, 0x18000
	s_mov_b32 s7, m0
	s_mov_b32 m0, s83
	s_nop 0
	global_load_lds_dwordx4 v145, s[4:5]
	s_mov_b32 m0, s7
	s_add_i32 s84, s15, 0x1a000
	s_mov_b32 s7, m0
	s_mov_b32 m0, s84
	s_nop 0
	global_load_lds_dwordx4 v155, s[4:5]
	s_mov_b32 m0, s7
	s_add_u32 s4, s18, 0x80
	s_addc_u32 s5, s19, 0
	s_add_i32 s85, s15, 0x8000
	s_mov_b32 s7, m0
	s_mov_b32 m0, s85
	s_nop 0
	global_load_lds_dwordx4 v129, s[4:5]
	s_mov_b32 m0, s7
	s_add_i32 s86, s15, 0xa000
	s_mov_b32 s7, m0
	s_mov_b32 m0, s86
	s_nop 0
	global_load_lds_dwordx4 v154, s[4:5]
	s_mov_b32 m0, s7
	s_add_u32 s4, s22, 0x80080
	s_addc_u32 s5, s23, 0
	s_add_i32 s87, s15, 0x1c000
	s_mov_b32 s7, m0
	s_mov_b32 m0, s87
	s_nop 0
	global_load_lds_dwordx4 v145, s[4:5]
	s_mov_b32 m0, s7
	s_add_i32 s88, s15, 0x1e000
	s_add_i32 s89, s15, 0xc000
	s_mov_b32 s7, m0
	s_mov_b32 m0, s88
	s_nop 0
	global_load_lds_dwordx4 v155, s[4:5]
	s_mov_b32 m0, s7
	s_cmpk_lt_u32 s28, 0x100
	s_cselect_b64 s[26:27], -1, 0
	s_lshl_b32 s7, s6, 4
	s_add_i32 s90, s15, 0xe000
	s_lshl_b32 s4, s6, 6
	s_add_u32 s4, s12, s4
	v_mov_b32_e32 v131, 0
	s_addc_u32 s5, s13, 0
	v_lshlrev_b32_e32 v128, 3, v2
	v_lshlrev_b32_e32 v0, 2, v2
	v_lshl_add_u64 v[2:3], s[4:5], 0, v[130:131]
	s_mov_b64 s[4:5], 0x1db00000
	v_lshl_add_u64 v[132:133], v[2:3], 0, s[4:5]
	s_mov_b64 s[4:5], 0x10a00000
	s_waitcnt vmcnt(6)
	v_lshl_add_u64 v[134:135], v[2:3], 0, s[4:5]
	s_mov_b64 s[4:5], 0x100000
	v_lshl_add_u64 v[136:137], v[2:3], 0, s[4:5]
	s_mov_b64 s[4:5], 0x180000
	v_lshl_add_u64 v[138:139], v[2:3], 0, s[4:5]
	v_add_u32_e32 v157, 0, v1
	v_add_u32_e32 v158, 0, v4
	s_mov_b64 s[28:29], 0xa0000
	s_mov_b32 s91, 0xa0000
	s_mov_b64 s[40:41], 0xb0000
	s_mov_b32 s92, 0xb0000
	s_mov_b32 s93, 0x40000
	s_mov_b64 s[44:45], 0x48000
	s_mov_b32 s94, 0x48000
	s_mov_b64 s[46:47], 0x50000
	s_mov_b32 s95, 0x50000
	s_mov_b64 s[48:49], 0x58000
	s_mov_b32 s96, 0x58000
	s_lshl_b32 s4, s7, 1
	v_lshlrev_b32_e32 v140, 1, v0
	v_mov_b32_e32 v159, 0x3db504f3
	s_mov_b32 s36, 0
	v_mov_b32_e32 v124, 0
	v_mov_b32_e32 v125, 0
	v_mov_b32_e32 v126, 0
	v_mov_b32_e32 v127, 0
	s_nop 1
	v_mfma_f32_32x32x16_bf16 v[0:15], v[124:127], v[124:127], 0
	v_mfma_f32_32x32x16_bf16 v[16:31], v[124:127], v[124:127], 0
	v_mfma_f32_32x32x16_bf16 v[32:47], v[124:127], v[124:127], 0
	v_mfma_f32_32x32x16_bf16 v[48:63], v[124:127], v[124:127], 0
	v_mfma_f32_32x32x16_bf16 v[64:79], v[124:127], v[124:127], 0
	v_mfma_f32_32x32x16_bf16 v[80:95], v[124:127], v[124:127], 0
	v_mfma_f32_32x32x16_bf16 v[96:111], v[124:127], v[124:127], 0
	v_mfma_f32_16x16x32_bf16 v[112:115], v[124:127], v[124:127], 0
	v_mfma_f32_16x16x32_bf16 v[116:119], v[124:127], v[124:127], 0
	v_mfma_f32_16x16x32_bf16 v[120:123], v[124:127], v[124:127], 0
	s_waitcnt vmcnt(20)
	s_waitcnt vmcnt(19)
	s_waitcnt vmcnt(18)
	s_waitcnt vmcnt(17)
	s_waitcnt vmcnt(16)
	s_waitcnt vmcnt(15)
	s_waitcnt vmcnt(14)
	s_waitcnt vmcnt(13)
	s_waitcnt vmcnt(12)
	s_waitcnt vmcnt(11)
	s_waitcnt vmcnt(10)
	s_waitcnt vmcnt(9)
	s_waitcnt vmcnt(8)
	s_barrier
	v_writelane_b32 v254, s4, 3
	s_branch .LBB0_229
.LBB0_227:
	v_mov_b32_e32 v0, 0
	s_mov_b32 s14, s50
	s_mov_b32 s16, s52
	s_mov_b32 s77, s67
	s_mov_b64 s[22:23], s[54:55]
	s_mov_b64 s[18:19], s[8:9]
	s_mov_b32 s36, s37
	v_mov_b32_e32 v124, 0
	v_mov_b32_e32 v125, 0
	v_mov_b32_e32 v126, 0
	v_mov_b32_e32 v127, 0
	s_nop 1
	v_mfma_f32_32x32x16_bf16 v[0:15], v[124:127], v[124:127], 0
	v_mfma_f32_32x32x16_bf16 v[16:31], v[124:127], v[124:127], 0
	v_mfma_f32_32x32x16_bf16 v[32:47], v[124:127], v[124:127], 0
	v_mfma_f32_32x32x16_bf16 v[48:63], v[124:127], v[124:127], 0
	v_mfma_f32_32x32x16_bf16 v[64:79], v[124:127], v[124:127], 0
	v_mfma_f32_32x32x16_bf16 v[80:95], v[124:127], v[124:127], 0
	v_mfma_f32_32x32x16_bf16 v[96:111], v[124:127], v[124:127], 0
	v_mfma_f32_16x16x32_bf16 v[112:115], v[124:127], v[124:127], 0
	v_mfma_f32_16x16x32_bf16 v[116:119], v[124:127], v[124:127], 0
	v_mfma_f32_16x16x32_bf16 v[120:123], v[124:127], v[124:127], 0

;     DI int nt(const Unit& u) const { return (u.aux & 8) ? PLED / 64 : ((u.aux & 4) ? (D_ / 2) / 64 : D_ / 64); }
; template <class Epi, class Sched, bool ALIGN_EPI, bool FP8 = false>
; DI void gemm_phase(LAS unsigned char* lds, const Gemm g, const Sched& S, const Epi& E) {
;     ...
; #pragma unroll
;         for (int a = 0; a < 2; ++a)
; #pragma unroll
;             for (int b = 0; b < 2; ++b)
; #pragma unroll
;                 for (int m = 0; m < 4; ++m)
; #pragma unroll
;                     for (int n = 0; n < 2; ++n) acc[a][b][m][n] = (f32x4){0.f, 0.f, 0.f, 0.f};
;         cur = nxt; cA = nA; cB = nB; ++ui;
;         if constexpr (sched_vark<Sched>::value) nt = S.nt(cur);
.LBB0_297:
	s_ashr_i32 s43, s42, 31
	s_lshl_b64 s[44:45], s[42:43], 19
	s_add_u32 s44, s36, s44
	s_addc_u32 s45, s37, s45
	s_and_b64 s[46:47], s[4:5], exec
	s_cselect_b32 s43, s45, s51
	s_cselect_b32 s87, s44, s50
	s_ashr_i32 s41, s40, 31
	s_lshl_b64 s[46:47], s[40:41], 19
	s_add_u32 s46, s39, s46
	s_addc_u32 s47, s60, s47
	s_and_b64 s[54:55], s[4:5], exec
	s_cselect_b32 s41, s47, s53
	s_cselect_b32 s88, s46, s52
	s_add_u32 s89, s52, 0x100
	v_mov_b32_e32 v140, 0
	v_mov_b32_e32 v141, 0
	v_mov_b32_e32 v142, 0
	v_mov_b32_e32 v143, 0
	s_nop 1
	v_mfma_f32_32x32x16_bf16 v[0:15], v[140:143], v[140:143], 0
	v_mfma_f32_32x32x16_bf16 v[16:31], v[140:143], v[140:143], 0
	v_mfma_f32_32x32x16_bf16 v[32:47], v[140:143], v[140:143], 0
	v_mfma_f32_32x32x16_bf16 v[48:63], v[140:143], v[140:143], 0
	v_mfma_f32_32x32x16_bf16 v[64:79], v[140:143], v[140:143], 0
	v_mfma_f32_32x32x16_bf16 v[80:95], v[140:143], v[140:143], 0
	v_mfma_f32_16x16x32_bf16 v[96:99], v[140:143], v[140:143], 0
	v_mfma_f32_16x16x32_bf16 v[100:103], v[140:143], v[140:143], 0
	v_mfma_f32_16x16x32_bf16 v[120:123], v[140:143], v[140:143], 0
	v_mfma_f32_16x16x32_bf16 v[124:127], v[140:143], v[140:143], 0
	v_mfma_f32_16x16x32_bf16 v[128:131], v[140:143], v[140:143], 0
	v_mfma_f32_16x16x32_bf16 v[132:135], v[140:143], v[140:143], 0
	v_mfma_f32_16x16x32_bf16 v[136:139], v[140:143], v[140:143], 0
	s_addc_u32 s90, s53, 0
	s_mov_b32 s91, -2
	s_waitcnt vmcnt(19)
	s_waitcnt vmcnt(18)
	s_waitcnt vmcnt(15)
	s_waitcnt vmcnt(14)
	s_waitcnt vmcnt(13)
	s_waitcnt vmcnt(12)
	s_waitcnt vmcnt(11)
	s_waitcnt vmcnt(9)
	.p2alignl 6, 3212836864

; #define PG8_BAR __builtin_amdgcn_s_barrier()
;     DI int nt(const Unit& u) const { return (u.aux & 8) ? PLED / 64 : ((u.aux & 4) ? (D_ / 2) / 64 : D_ / 64); }
; template <class Epi, class Sched, bool ALIGN_EPI, bool FP8 = false>
; DI void gemm_phase(LAS unsigned char* lds, const Gemm g, const Sched& S, const Epi& E) {
;     ...
; #pragma unroll
;         for (int a = 0; a < 2; ++a)
; #pragma unroll
;             for (int b = 0; b < 2; ++b)
; #pragma unroll
;                 for (int m = 0; m < 4; ++m)
; #pragma unroll
;                     for (int n = 0; n < 2; ++n) acc[a][b][m][n] = (f32x4){0.f, 0.f, 0.f, 0.f};
;         cur = nxt; cA = nA; cB = nB; ++ui;
;         if constexpr (sched_vark<Sched>::value) nt = S.nt(cur);
;         if constexpr (ALIGN_EPI) { if (wr == 1) PG8_BAR; }
.LBB0_568:
	s_ashr_i32 s57, s56, 31
	s_lshl_b64 s[58:59], s[56:57], 20
	s_add_u32 s58, s17, s58
	s_addc_u32 s59, s35, s59
	s_and_b64 s[60:61], s[4:5], exec
	s_cselect_b32 s57, s59, s65
	s_cselect_b32 s93, s58, s64
	s_ashr_i32 s55, s54, 31
	s_lshl_b64 s[60:61], s[54:55], 20
	s_add_u32 s60, s36, s60
	s_addc_u32 s61, s37, s61
	s_and_b64 s[68:69], s[4:5], exec
	s_cselect_b32 s55, s61, s67
	s_cselect_b32 s94, s60, s66
	s_add_u32 s95, s66, 0x100
	v_mov_b32_e32 v124, 0
	v_mov_b32_e32 v125, 0
	v_mov_b32_e32 v126, 0
	v_mov_b32_e32 v127, 0
	s_nop 1
	v_mfma_f32_32x32x16_bf16 v[0:15], v[124:127], v[124:127], 0
	v_mfma_f32_32x32x16_bf16 v[16:31], v[124:127], v[124:127], 0
	v_mfma_f32_32x32x16_bf16 v[32:47], v[124:127], v[124:127], 0
	v_mfma_f32_32x32x16_bf16 v[48:63], v[124:127], v[124:127], 0
	v_mfma_f32_32x32x16_bf16 v[64:79], v[124:127], v[124:127], 0
	v_mfma_f32_32x32x16_bf16 v[80:95], v[124:127], v[124:127], 0
	v_mfma_f32_32x32x16_bf16 v[96:111], v[124:127], v[124:127], 0
	v_mfma_f32_16x16x32_bf16 v[112:115], v[124:127], v[124:127], 0
	v_mfma_f32_16x16x32_bf16 v[116:119], v[124:127], v[124:127], 0
	v_mfma_f32_16x16x32_bf16 v[120:123], v[124:127], v[124:127], 0
	s_addc_u32 s96, s67, 0
	s_mov_b32 s97, -2
	s_waitcnt vmcnt(15)
	s_waitcnt vmcnt(14)
	s_waitcnt vmcnt(13)
	s_waitcnt vmcnt(12)
	s_waitcnt vmcnt(11)
	s_waitcnt vmcnt(9)
	s_waitcnt vmcnt(8)
	.p2alignl 6, 3212836864

; #define PG8_BAR __builtin_amdgcn_s_barrier()
;     DI int nt(const Unit& u) const { return (u.aux & 8) ? PLED / 64 : ((u.aux & 4) ? (D_ / 2) / 64 : D_ / 64); }
; template <class Epi, class Sched, bool ALIGN_EPI, bool FP8 = false>
; DI void gemm_phase(LAS unsigned char* lds, const Gemm g, const Sched& S, const Epi& E) {
;     ...
; #pragma unroll
;         for (int a = 0; a < 2; ++a)
; #pragma unroll
;             for (int b = 0; b < 2; ++b)
; #pragma unroll
;                 for (int m = 0; m < 4; ++m)
; #pragma unroll
;                     for (int n = 0; n < 2; ++n) acc[a][b][m][n] = (f32x4){0.f, 0.f, 0.f, 0.f};
;         cur = nxt; cA = nA; cB = nB; ++ui;
;         if constexpr (sched_vark<Sched>::value) nt = S.nt(cur);
;         if constexpr (ALIGN_EPI) { if (wr == 1) PG8_BAR; }
.LBB0_699:
	s_ashr_i32 s17, s16, 31
	s_lshl_b64 s[18:19], s[16:17], 20
	s_add_u32 s18, s3, s18
	s_addc_u32 s19, s35, s19
	s_and_b64 s[20:21], s[4:5], exec
	s_cselect_b32 s17, s19, s25
	s_cselect_b32 s67, s18, s24
	s_ashr_i32 s13, s12, 31
	s_lshl_b64 s[20:21], s[12:13], 20
	s_add_u32 s20, s36, s20
	s_addc_u32 s21, s37, s21
	s_and_b64 s[28:29], s[4:5], exec
	s_cselect_b32 s13, s21, s27
	s_cselect_b32 s68, s20, s26
	s_add_u32 s69, s26, 0x100
	v_mov_b32_e32 v124, 0
	v_mov_b32_e32 v125, 0
	v_mov_b32_e32 v126, 0
	v_mov_b32_e32 v127, 0
	s_nop 1
	v_mfma_f32_32x32x16_bf16 v[0:15], v[124:127], v[124:127], 0
	v_mfma_f32_32x32x16_bf16 v[16:31], v[124:127], v[124:127], 0
	v_mfma_f32_32x32x16_bf16 v[32:47], v[124:127], v[124:127], 0
	v_mfma_f32_32x32x16_bf16 v[48:63], v[124:127], v[124:127], 0
	v_mfma_f32_32x32x16_bf16 v[64:79], v[124:127], v[124:127], 0
	v_mfma_f32_32x32x16_bf16 v[80:95], v[124:127], v[124:127], 0
	v_mfma_f32_32x32x16_bf16 v[96:111], v[124:127], v[124:127], 0
	v_mfma_f32_16x16x32_bf16 v[112:115], v[124:127], v[124:127], 0
	v_mfma_f32_16x16x32_bf16 v[116:119], v[124:127], v[124:127], 0
	v_mfma_f32_16x16x32_bf16 v[120:123], v[124:127], v[124:127], 0
	s_addc_u32 s70, s27, 0
	s_mov_b32 s71, -2
	.p2alignl 6, 3212836864

; #define PG8_BAR __builtin_amdgcn_s_barrier()
;     DI int nt(const Unit& u) const { return (u.aux & 8) ? PLED / 64 : ((u.aux & 4) ? (D_ / 2) / 64 : D_ / 64); }
; template <class Epi, class Sched, bool ALIGN_EPI, bool FP8 = false>
; DI void gemm_phase(LAS unsigned char* lds, const Gemm g, const Sched& S, const Epi& E) {
;     ...
; #pragma unroll
;         for (int a = 0; a < 2; ++a)
; #pragma unroll
;             for (int b = 0; b < 2; ++b)
; #pragma unroll
;                 for (int m = 0; m < 4; ++m)
; #pragma unroll
;                     for (int n = 0; n < 2; ++n) acc[a][b][m][n] = (f32x4){0.f, 0.f, 0.f, 0.f};
;         cur = nxt; cA = nA; cB = nB; ++ui;
;         if constexpr (sched_vark<Sched>::value) nt = S.nt(cur);
;         if constexpr (ALIGN_EPI) { if (wr == 1) PG8_BAR; }
.LBB0_723:
	s_ashr_i32 s57, s56, 31
	s_lshl_b64 s[58:59], s[56:57], 20
	s_add_u32 s58, s3, s58
	s_addc_u32 s59, s35, s59
	s_and_b64 s[60:61], s[4:5], exec
	s_cselect_b32 s57, s59, s65
	s_cselect_b32 s94, s58, s64
	s_ashr_i32 s55, s54, 31
	s_lshl_b64 s[60:61], s[54:55], 20
	s_add_u32 s60, s37, s60
	s_addc_u32 s61, s39, s61
	s_and_b64 s[68:69], s[4:5], exec
	s_cselect_b32 s55, s61, s67
	s_cselect_b32 s95, s60, s66
	s_add_u32 s96, s66, 0x100
	v_mov_b32_e32 v124, 0
	v_mov_b32_e32 v125, 0
	v_mov_b32_e32 v126, 0
	v_mov_b32_e32 v127, 0
	s_nop 1
	v_mfma_f32_32x32x16_bf16 v[0:15], v[124:127], v[124:127], 0
	v_mfma_f32_32x32x16_bf16 v[16:31], v[124:127], v[124:127], 0
	v_mfma_f32_32x32x16_bf16 v[32:47], v[124:127], v[124:127], 0
	v_mfma_f32_32x32x16_bf16 v[48:63], v[124:127], v[124:127], 0
	v_mfma_f32_32x32x16_bf16 v[64:79], v[124:127], v[124:127], 0
	v_mfma_f32_32x32x16_bf16 v[80:95], v[124:127], v[124:127], 0
	v_mfma_f32_32x32x16_bf16 v[96:111], v[124:127], v[124:127], 0
	v_mfma_f32_16x16x32_bf16 v[112:115], v[124:127], v[124:127], 0
	v_mfma_f32_16x16x32_bf16 v[116:119], v[124:127], v[124:127], 0
	v_mfma_f32_16x16x32_bf16 v[120:123], v[124:127], v[124:127], 0
	s_addc_u32 s97, s67, 0
	s_mov_b32 vcc_lo, -2
	s_waitcnt vmcnt(15)
	s_waitcnt vmcnt(14)
	s_waitcnt vmcnt(13)
	s_waitcnt vmcnt(12)
	s_waitcnt vmcnt(11)
	s_waitcnt vmcnt(9)
	s_waitcnt vmcnt(8)
	.p2alignl 6, 3212836864

; #define PG8_BAR __builtin_amdgcn_s_barrier()
;     DI int nt(const Unit& u) const { return (u.aux & 8) ? PLED / 64 : ((u.aux & 4) ? (D_ / 2) / 64 : D_ / 64); }
; template <class Epi, class Sched, bool ALIGN_EPI, bool FP8 = false>
; DI void gemm_phase(LAS unsigned char* lds, const Gemm g, const Sched& S, const Epi& E) {
;     ...
; #pragma unroll
;         for (int a = 0; a < 2; ++a)
; #pragma unroll
;             for (int b = 0; b < 2; ++b)
; #pragma unroll
;                 for (int m = 0; m < 4; ++m)
; #pragma unroll
;                     for (int n = 0; n < 2; ++n) acc[a][b][m][n] = (f32x4){0.f, 0.f, 0.f, 0.f};
;         cur = nxt; cA = nA; cB = nB; ++ui;
;         if constexpr (sched_vark<Sched>::value) nt = S.nt(cur);
;         if constexpr (ALIGN_EPI) { if (wr == 1) PG8_BAR; }
.LBB0_808:
	s_add_u32 s81, s50, 0x100
	v_mov_b32_e32 v124, 0
	v_mov_b32_e32 v125, 0
	v_mov_b32_e32 v126, 0
	v_mov_b32_e32 v127, 0
	s_nop 1
	v_mfma_f32_32x32x16_bf16 v[0:15], v[124:127], v[124:127], 0
	v_mfma_f32_32x32x16_bf16 v[16:31], v[124:127], v[124:127], 0
	v_mfma_f32_32x32x16_bf16 v[32:47], v[124:127], v[124:127], 0
	v_mfma_f32_32x32x16_bf16 v[48:63], v[124:127], v[124:127], 0
	v_mfma_f32_32x32x16_bf16 v[64:79], v[124:127], v[124:127], 0
	v_mfma_f32_32x32x16_bf16 v[80:95], v[124:127], v[124:127], 0
	v_mfma_f32_32x32x16_bf16 v[96:111], v[124:127], v[124:127], 0
	v_mfma_f32_16x16x32_bf16 v[112:115], v[124:127], v[124:127], 0
	v_mfma_f32_16x16x32_bf16 v[116:119], v[124:127], v[124:127], 0
	v_mfma_f32_16x16x32_bf16 v[120:123], v[124:127], v[124:127], 0
	s_addc_u32 s82, s51, 0
	s_mov_b32 s83, -2
	s_waitcnt vmcnt(19)
	s_waitcnt vmcnt(18)
	s_waitcnt vmcnt(15)
	s_waitcnt vmcnt(14)
	s_waitcnt vmcnt(13)
	s_waitcnt vmcnt(12)
	s_waitcnt vmcnt(11)
	s_waitcnt vmcnt(9)
	s_waitcnt vmcnt(8)
	.p2alignl 6, 3212836864

; #define LAS __attribute__((address_space(3)))
; template <class Epi, class Sched, bool ALIGN_EPI, bool FP8 = false>
; DI void gemm_phase(LAS unsigned char* lds, const Gemm g, const Sched& S, const Epi& E) {
;     ...
;     const int wid = __builtin_amdgcn_readfirstlane(tid >> 6), lane = tid & 63, wr = wid >> 2, wc = wid & 3, fr = lane & 15, fq = lane >> 4;
;     const int K = g.K; int nt = K / BK;
;     unsigned voffA[2], voffB[2];
; #pragma unroll
;     for (int i = 0; i < 2; ++i) { int R, C; stage_rc(tid * 16 + i * 8192, R, C); const int Rb = Epi::PERM ? ((R & ~31) + perm32(R & 31)) : R;
;         voffA[i] = (unsigned)(R * g.lda + C) * 2u; voffB[i] = (unsigned)(Rb * g.ldb + C) * 2u; }
;     const size_t kstep = (size_t)(BK * 2);
;     const size_t hstepA = (size_t)HALF * g.lda * 2, hstepB = (size_t)HALF * g.ldb * 2;
;     const unsigned ldsw = (unsigned)wid * 1024u;
;     const unsigned ldsbase = (unsigned)__builtin_amdgcn_readfirstlane((int)(unsigned)(size_t)lds) + ldsw;
;     const int aoff = lds_byte(wr * 64 + fr, fq * 8), boff = lds_byte(wc * 32 + fr, fq * 8);
;     const int aoff8a = lds_byte(wr * 64 + fr, fq * 16), boff8a = lds_byte(wc * 32 + fr, fq * 16);
;     const LAS unsigned char* a8base = lds + aoff8a; const LAS unsigned char* b8base = lds + 4 * HTB + boff8a;
;     if constexpr (FP8) { asm volatile("" : "+v"(a8base)); asm volatile("" : "+v"(b8base)); }
;     static_assert(lds_byte(9, 24) == lds_byte(9, 16) + 16 && lds_byte(3, 56) == lds_byte(3, 48) + 16, "fp8 fragment pieces are adjacent");
;     ...
;     Unit cur, nxt; int ui = 0;
;     if (!S.next(0, cur)) return;
;     if constexpr (sched_vark<Sched>::value) nt = S.nt(cur);
;     f32x4 acc[2][2][4][2];
; #pragma unroll
;     for (int a = 0; a < 2; ++a)
; #pragma unroll
;         for (int b = 0; b < 2; ++b)
; #pragma unroll
;             for (int m = 0; m < 4; ++m)
; #pragma unroll
;                 for (int n = 0; n < 2; ++n) acc[a][b][m][n] = (f32x4){0.f, 0.f, 0.f, 0.f};
;     bf16x8 At[4][2], B0[2][2], B1[2][2]; v8i At8[4], B08[2], B18[2];
;     const char* cA = (const char*)g.A + S.a_off(cur); const char* cB = (const char*)g.Bt + S.b_off(cur);
;     PG8_STAGE(PG8_SB(0, 0), cB, voffB); PG8_STAGE(PG8_SB(0, 1), cB + hstepB, voffB); PG8_STAGE(PG8_SA(0, 0), cA, voffA); PG8_STAGE(PG8_SA(0, 1), cA + hstepA, voffA);
;     if (wr == 1) PG8_BAR;
;     PG8_WAIT_V(2); PG8_BAR;
.LBB0_962:
	s_and_b64 s[4:5], s[4:5], exec
	s_cselect_b32 s20, 32, 16
	s_and_b64 s[4:5], s[6:7], exec
	s_cselect_b32 s81, s20, 4
	s_add_u32 s74, s12, 0x18b00000
	s_addc_u32 s75, s13, 0
	v_bfe_u32 v2, v0, 4, 2
	s_add_u32 s79, s12, 0x1ab00000
	v_and_b32_e32 v1, 15, v0
	v_lshlrev_b32_e32 v130, 4, v2
	v_lshlrev_b32_e32 v0, 2, v0
	s_addc_u32 s80, s13, 0
	s_and_b32 s6, s8, 3
	v_lshl_or_b32 v156, s9, 6, v1
	s_lshl_b32 s4, s9, 13
	v_lshl_or_b32 v1, v1, 6, v130
	v_and_b32_e32 v0, 32, v0
	v_bitop3_b32 v4, v1, s4, v0 bitop3:0xde
	s_lshl_b32 s82, s6, 5
	s_lshl_b32 s4, s6, 12
	v_bitop3_b32 v1, v1, s4, v0 bitop3:0xde
	s_add_u32 s4, s22, 0x80
	s_waitcnt vmcnt(2)
	s_barrier
	s_addc_u32 s5, s23, 0
	s_add_i32 s83, s15, 0x18000
	s_mov_b32 s7, m0
	s_mov_b32 m0, s83
	s_nop 0
	global_load_lds_dwordx4 v145, s[4:5]
	s_mov_b32 m0, s7
	s_add_i32 s84, s15, 0x1a000
	s_mov_b32 s7, m0
	s_mov_b32 m0, s84
	s_nop 0
	global_load_lds_dwordx4 v155, s[4:5]
	s_mov_b32 m0, s7
	s_add_u32 s4, s18, 0x80
	s_addc_u32 s5, s19, 0
	s_add_i32 s85, s15, 0x8000
	s_mov_b32 s7, m0
	s_mov_b32 m0, s85
	s_nop 0
	global_load_lds_dwordx4 v129, s[4:5]
	s_mov_b32 m0, s7
	s_add_i32 s86, s15, 0xa000
	s_mov_b32 s7, m0
	s_mov_b32 m0, s86
	s_nop 0
	global_load_lds_dwordx4 v154, s[4:5]
	s_mov_b32 m0, s7
	s_add_u32 s4, s22, 0x80080
	s_addc_u32 s5, s23, 0
	s_add_i32 s87, s15, 0x1c000
	s_mov_b32 s7, m0
	s_mov_b32 m0, s87
	s_nop 0
	global_load_lds_dwordx4 v145, s[4:5]
	s_mov_b32 m0, s7
	s_add_i32 s88, s15, 0x1e000
	s_add_i32 s89, s15, 0xc000
	s_mov_b32 s7, m0
	s_mov_b32 m0, s88
	s_nop 0
	global_load_lds_dwordx4 v155, s[4:5]
	s_mov_b32 m0, s7
	s_cmpk_lt_u32 s28, 0x100
	s_cselect_b64 s[26:27], -1, 0
	s_lshl_b32 s7, s6, 4
	s_add_i32 s90, s15, 0xe000
	s_lshl_b32 s4, s6, 6
	s_add_u32 s4, s12, s4
	v_mov_b32_e32 v131, 0
	s_addc_u32 s5, s13, 0
	v_lshlrev_b32_e32 v128, 3, v2
	v_lshlrev_b32_e32 v0, 2, v2
	v_lshl_add_u64 v[2:3], s[4:5], 0, v[130:131]
	s_mov_b64 s[4:5], 0x1db00000
	v_lshl_add_u64 v[132:133], v[2:3], 0, s[4:5]
	s_mov_b64 s[4:5], 0x10a00000
	s_waitcnt vmcnt(6)
	v_lshl_add_u64 v[134:135], v[2:3], 0, s[4:5]
	s_mov_b64 s[4:5], 0x100000
	v_lshl_add_u64 v[136:137], v[2:3], 0, s[4:5]
	s_mov_b64 s[4:5], 0x180000
	v_lshl_add_u64 v[138:139], v[2:3], 0, s[4:5]
	v_add_u32_e32 v157, 0, v1
	v_add_u32_e32 v158, 0, v4
	s_mov_b64 s[28:29], 0xa0000
	s_mov_b32 s91, 0xa0000
	s_mov_b64 s[40:41], 0xb0000
	s_mov_b32 s92, 0xb0000
	s_mov_b32 s93, 0x40000
	s_mov_b64 s[44:45], 0x48000
	s_mov_b32 s94, 0x48000
	s_mov_b64 s[46:47], 0x50000
	s_mov_b32 s95, 0x50000
	s_mov_b64 s[48:49], 0x58000
	s_mov_b32 s96, 0x58000
	s_lshl_b32 s4, s7, 1
	v_lshlrev_b32_e32 v140, 1, v0
	v_mov_b32_e32 v159, 0x3db504f3
	s_mov_b32 s36, 0
	v_mov_b32_e32 v124, 0
	v_mov_b32_e32 v125, 0
	v_mov_b32_e32 v126, 0
	v_mov_b32_e32 v127, 0
	s_nop 1
	v_mfma_f32_32x32x16_bf16 v[0:15], v[124:127], v[124:127], 0
	v_mfma_f32_32x32x16_bf16 v[16:31], v[124:127], v[124:127], 0
	v_mfma_f32_32x32x16_bf16 v[32:47], v[124:127], v[124:127], 0
	v_mfma_f32_32x32x16_bf16 v[48:63], v[124:127], v[124:127], 0
	v_mfma_f32_32x32x16_bf16 v[64:79], v[124:127], v[124:127], 0
	v_mfma_f32_32x32x16_bf16 v[80:95], v[124:127], v[124:127], 0
	v_mfma_f32_32x32x16_bf16 v[96:111], v[124:127], v[124:127], 0
	v_mfma_f32_16x16x32_bf16 v[112:115], v[124:127], v[124:127], 0
	v_mfma_f32_16x16x32_bf16 v[116:119], v[124:127], v[124:127], 0
	v_mfma_f32_16x16x32_bf16 v[120:123], v[124:127], v[124:127], 0
	s_waitcnt vmcnt(15)
	s_waitcnt vmcnt(14)
	s_waitcnt vmcnt(13)
	s_waitcnt vmcnt(12)
	s_waitcnt vmcnt(11)
	s_waitcnt vmcnt(10)
	s_waitcnt vmcnt(9)
	s_waitcnt vmcnt(8)
	s_barrier
	v_writelane_b32 v254, s4, 3
	s_branch .LBB0_965
.LBB0_963:
	v_mov_b32_e32 v0, 0
	s_mov_b32 s14, s50
	s_mov_b32 s16, s52
	s_mov_b32 s67, s77
	s_mov_b64 s[22:23], s[54:55]
	s_mov_b64 s[18:19], s[8:9]
	s_mov_b32 s36, s37
	v_mov_b32_e32 v124, 0
	v_mov_b32_e32 v125, 0
	v_mov_b32_e32 v126, 0
	v_mov_b32_e32 v127, 0
	s_nop 1
	v_mfma_f32_32x32x16_bf16 v[0:15], v[124:127], v[124:127], 0
	v_mfma_f32_32x32x16_bf16 v[16:31], v[124:127], v[124:127], 0
	v_mfma_f32_32x32x16_bf16 v[32:47], v[124:127], v[124:127], 0
	v_mfma_f32_32x32x16_bf16 v[48:63], v[124:127], v[124:127], 0
	v_mfma_f32_32x32x16_bf16 v[64:79], v[124:127], v[124:127], 0
	v_mfma_f32_32x32x16_bf16 v[80:95], v[124:127], v[124:127], 0
	v_mfma_f32_32x32x16_bf16 v[96:111], v[124:127], v[124:127], 0
	v_mfma_f32_16x16x32_bf16 v[112:115], v[124:127], v[124:127], 0
	v_mfma_f32_16x16x32_bf16 v[116:119], v[124:127], v[124:127], 0
	v_mfma_f32_16x16x32_bf16 v[120:123], v[124:127], v[124:127], 0

; #define PG8_BAR __builtin_amdgcn_s_barrier()
;     DI int nt(const Unit& u) const { return (u.aux & 8) ? PLED / 64 : ((u.aux & 4) ? (D_ / 2) / 64 : D_ / 64); }
; template <class Epi, class Sched, bool ALIGN_EPI, bool FP8 = false>
; DI void gemm_phase(LAS unsigned char* lds, const Gemm g, const Sched& S, const Epi& E) {
;     ...
; #pragma unroll
;         for (int a = 0; a < 2; ++a)
; #pragma unroll
;             for (int b = 0; b < 2; ++b)
; #pragma unroll
;                 for (int m = 0; m < 4; ++m)
; #pragma unroll
;                     for (int n = 0; n < 2; ++n) acc[a][b][m][n] = (f32x4){0.f, 0.f, 0.f, 0.f};
;         cur = nxt; cA = nA; cB = nB; ++ui;
;         if constexpr (sched_vark<Sched>::value) nt = S.nt(cur);
;         if constexpr (ALIGN_EPI) { if (wr == 1) PG8_BAR; }
.LBB0_1607:
	s_ashr_i32 s17, s16, 31
	s_lshl_b64 s[20:21], s[16:17], 19
	s_add_u32 s20, s35, s20
	s_addc_u32 s21, s36, s21
	s_and_b64 s[6:7], s[6:7], exec
	s_cselect_b32 s15, s21, s27
	s_cselect_b32 s17, s20, s26
	s_add_u32 s68, s28, 0x100
	v_mov_b32_e32 v124, 0
	v_mov_b32_e32 v125, 0
	v_mov_b32_e32 v126, 0
	v_mov_b32_e32 v127, 0
	s_nop 1
	v_mfma_f32_32x32x16_bf16 v[0:15], v[124:127], v[124:127], 0
	v_mfma_f32_32x32x16_bf16 v[16:31], v[124:127], v[124:127], 0
	v_mfma_f32_32x32x16_bf16 v[32:47], v[124:127], v[124:127], 0
	v_mfma_f32_32x32x16_bf16 v[48:63], v[124:127], v[124:127], 0
	v_mfma_f32_32x32x16_bf16 v[64:79], v[124:127], v[124:127], 0
	v_mfma_f32_32x32x16_bf16 v[80:95], v[124:127], v[124:127], 0
	v_mfma_f32_32x32x16_bf16 v[96:111], v[124:127], v[124:127], 0
	v_mfma_f32_16x16x32_bf16 v[112:115], v[124:127], v[124:127], 0
	v_mfma_f32_16x16x32_bf16 v[116:119], v[124:127], v[124:127], 0
	v_mfma_f32_16x16x32_bf16 v[120:123], v[124:127], v[124:127], 0
	s_addc_u32 s69, s29, 0
	s_mov_b32 s70, -2
	.p2alignl 6, 3212836864

; #define PG8_BAR __builtin_amdgcn_s_barrier()
;     DI int nt(const Unit& u) const { return (u.aux & 8) ? PLED / 64 : ((u.aux & 4) ? (D_ / 2) / 64 : D_ / 64); }
; template <class Epi, class Sched, bool ALIGN_EPI, bool FP8 = false>
; DI void gemm_phase(LAS unsigned char* lds, const Gemm g, const Sched& S, const Epi& E) {
;     ...
; #pragma unroll
;         for (int a = 0; a < 2; ++a)
; #pragma unroll
;             for (int b = 0; b < 2; ++b)
; #pragma unroll
;                 for (int m = 0; m < 4; ++m)
; #pragma unroll
;                     for (int n = 0; n < 2; ++n) acc[a][b][m][n] = (f32x4){0.f, 0.f, 0.f, 0.f};
;         cur = nxt; cA = nA; cB = nB; ++ui;
;         if constexpr (sched_vark<Sched>::value) nt = S.nt(cur);
;         if constexpr (ALIGN_EPI) { if (wr == 1) PG8_BAR; }
.LBB0_1684:
	s_add_u32 s90, s46, 0x100
	v_mov_b32_e32 v124, 0
	v_mov_b32_e32 v125, 0
	v_mov_b32_e32 v126, 0
	v_mov_b32_e32 v127, 0
	s_nop 1
	v_mfma_f32_32x32x16_bf16 v[0:15], v[124:127], v[124:127], 0
	v_mfma_f32_32x32x16_bf16 v[16:31], v[124:127], v[124:127], 0
	v_mfma_f32_32x32x16_bf16 v[32:47], v[124:127], v[124:127], 0
	v_mfma_f32_32x32x16_bf16 v[48:63], v[124:127], v[124:127], 0
	v_mfma_f32_32x32x16_bf16 v[64:79], v[124:127], v[124:127], 0
	v_mfma_f32_32x32x16_bf16 v[80:95], v[124:127], v[124:127], 0
	v_mfma_f32_32x32x16_bf16 v[96:111], v[124:127], v[124:127], 0
	v_mfma_f32_16x16x32_bf16 v[112:115], v[124:127], v[124:127], 0
	v_mfma_f32_16x16x32_bf16 v[116:119], v[124:127], v[124:127], 0
	v_mfma_f32_16x16x32_bf16 v[120:123], v[124:127], v[124:127], 0
	s_addc_u32 s91, s47, 0
	s_mov_b32 s92, -2
	.p2alignl 6, 3212836864

; #define PG8_BAR __builtin_amdgcn_s_barrier()
;     DI int nt(const Unit& u) const { return (u.aux & 8) ? PLED / 64 : ((u.aux & 4) ? (D_ / 2) / 64 : D_ / 64); }
; template <class Epi, class Sched, bool ALIGN_EPI, bool FP8 = false>
; DI void gemm_phase(LAS unsigned char* lds, const Gemm g, const Sched& S, const Epi& E) {
;     ...
; #pragma unroll
;         for (int a = 0; a < 2; ++a)
; #pragma unroll
;             for (int b = 0; b < 2; ++b)
; #pragma unroll
;                 for (int m = 0; m < 4; ++m)
; #pragma unroll
;                     for (int n = 0; n < 2; ++n) acc[a][b][m][n] = (f32x4){0.f, 0.f, 0.f, 0.f};
;         cur = nxt; cA = nA; cB = nB; ++ui;
;         if constexpr (sched_vark<Sched>::value) nt = S.nt(cur);
;         if constexpr (ALIGN_EPI) { if (wr == 1) PG8_BAR; }
.LBB0_1709:
	s_ashr_i32 s55, s54, 31
	s_lshl_b64 s[56:57], s[54:55], 20
	s_add_u32 s56, s36, s56
	s_addc_u32 s57, s37, s57
	s_and_b64 s[58:59], s[2:3], exec
	s_cselect_b32 s55, s57, s63
	s_cselect_b32 s94, s56, s62
	s_ashr_i32 s53, s52, 31
	s_lshl_b64 s[58:59], s[52:53], 20
	s_add_u32 s58, s39, s58
	s_addc_u32 s59, s72, s59
	s_and_b64 s[66:67], s[2:3], exec
	s_cselect_b32 s53, s59, s65
	s_cselect_b32 s95, s58, s64
	s_add_u32 s96, s64, 0x100
	v_mov_b32_e32 v124, 0
	v_mov_b32_e32 v125, 0
	v_mov_b32_e32 v126, 0
	v_mov_b32_e32 v127, 0
	s_nop 1
	v_mfma_f32_32x32x16_bf16 v[0:15], v[124:127], v[124:127], 0
	v_mfma_f32_32x32x16_bf16 v[16:31], v[124:127], v[124:127], 0
	v_mfma_f32_32x32x16_bf16 v[32:47], v[124:127], v[124:127], 0
	v_mfma_f32_32x32x16_bf16 v[48:63], v[124:127], v[124:127], 0
	v_mfma_f32_32x32x16_bf16 v[64:79], v[124:127], v[124:127], 0
	v_mfma_f32_32x32x16_bf16 v[80:95], v[124:127], v[124:127], 0
	v_mfma_f32_32x32x16_bf16 v[96:111], v[124:127], v[124:127], 0
	v_mfma_f32_16x16x32_bf16 v[112:115], v[124:127], v[124:127], 0
	v_mfma_f32_16x16x32_bf16 v[116:119], v[124:127], v[124:127], 0
	v_mfma_f32_16x16x32_bf16 v[120:123], v[124:127], v[124:127], 0
	s_addc_u32 s97, s65, 0
	s_mov_b32 vcc_lo, -2
	.p2alignl 6, 3212836864
